# v33
# baseline (speedup 1.0000x reference)
.LBB0_34:
	s_or_b64 exec, exec, s[10:11]
	ds_read_b128 v[18:21], v72
	s_waitcnt vmcnt(3)
	v_cvt_pk_f16_f32 v14, v14, v15
	v_cvt_pk_f16_f32 v15, v16, v17
	v_cvt_pk_f16_f32 v16, v10, v11
	ds_read_b128 v[22:25], v71 offset:41984
	v_cvt_pk_f16_f32 v17, v12, v13
	ds_read_b128 v[10:13], v72 offset:1024
	ds_read_b128 v[26:29], v71 offset:42048
	s_waitcnt vmcnt(1)
	v_cvt_pk_f16_f32 v0, v6, v7
	v_cvt_pk_f16_f32 v1, v8, v9
	v_cvt_pk_f16_f32 v2, v2, v3
	v_cvt_pk_f16_f32 v3, v4, v5
	s_waitcnt lgkmcnt(2)
	v_mfma_f32_16x16x32_f16 v[30:33], v[18:21], v[14:17], v[22:25]
	s_add_i32 s10, s20, s12
	v_mfma_f32_16x16x32_f16 v[18:21], v[18:21], v[0:3], v[22:25]
	ds_read_b128 v[4:7], v72 offset:2048
	s_nop 1
	ds_read_b128 v[22:25], v71 offset:42112
	s_waitcnt lgkmcnt(2)
	v_mfma_f32_16x16x32_f16 v[34:37], v[10:13], v[14:17], v[26:29]
	v_exp_f32_e32 v78, v30
	v_exp_f32_e32 v79, v31
	v_exp_f32_e32 v20, v20
	v_mfma_f32_16x16x32_f16 v[8:11], v[10:13], v[0:3], v[26:29]
	ds_read_b128 v[44:47], v71 offset:42176
	s_nop 2
	v_exp_f32_e64 v80, v34 clamp
	v_exp_f32_e64 v81, v35 clamp
	ds_read_b128 v[26:29], v72 offset:3072
	s_waitcnt lgkmcnt(2)
	v_mfma_f32_16x16x32_f16 v[48:51], v[4:7], v[14:17], v[22:25]
	v_exp_f32_e64 v82, v36 clamp
	v_exp_f32_e64 v83, v37 clamp
	v_exp_f32_e32 v21, v21
	v_mfma_f32_16x16x32_f16 v[22:25], v[4:7], v[0:3], v[22:25]
	ds_read_b128 v[52:55], v72 offset:4096
	ds_read_b128 v[56:59], v71 offset:42240
	s_nop 1
	v_exp_f32_e32 v4, v48
	s_waitcnt lgkmcnt(2)
	v_mfma_f32_16x16x32_f16 v[60:63], v[26:29], v[14:17], v[44:47]
	v_exp_f32_e32 v5, v49
	v_exp_f32_e32 v48, v32
	v_exp_f32_e32 v49, v33
	v_mfma_f32_16x16x32_f16 v[26:29], v[26:29], v[0:3], v[44:47]
	ds_read_b128 v[64:67], v71 offset:42304
	v_exp_f32_e32 v6, v50
	v_exp_f32_e32 v7, v51
	ds_read_b128 v[44:47], v72 offset:5120
	s_waitcnt lgkmcnt(2)
	v_mfma_f32_16x16x32_f16 v[74:77], v[52:55], v[14:17], v[56:59]
	v_exp_f32_e32 v50, v18
	v_exp_f32_e32 v51, v19
	v_exp_f32_e32 v26, v26
	v_mfma_f32_16x16x32_f16 v[30:33], v[52:55], v[0:3], v[56:59]
	v_exp_f32_e64 v52, v8 clamp
	v_exp_f32_e64 v53, v9 clamp
	v_exp_f32_e32 v8, v22
	s_waitcnt lgkmcnt(0)
	v_mfma_f32_16x16x32_f16 v[34:37], v[44:47], v[14:17], v[64:67]
	v_exp_f32_e32 v9, v23
	v_exp_f32_e64 v22, v10 clamp
	v_exp_f32_e64 v23, v11 clamp
	v_mfma_f32_16x16x32_f16 v[44:47], v[44:47], v[0:3], v[64:67]
	v_exp_f32_e32 v10, v24
	v_exp_f32_e32 v11, v25
	s_nop 1
	v_exp_f32_e32 v12, v34
	v_exp_f32_e32 v13, v35
	v_exp_f32_e32 v18, v36
	v_exp_f32_e32 v24, v60
	v_exp_f32_e32 v25, v61
	v_exp_f32_e64 v54, v74 clamp
	v_exp_f32_e64 v55, v75 clamp
	v_exp_f32_e32 v34, v62
	v_exp_f32_e32 v35, v63
	v_exp_f32_e64 v56, v76 clamp
	v_exp_f32_e64 v57, v77 clamp
	v_exp_f32_e32 v19, v37
	v_exp_f32_e32 v27, v27
	v_exp_f32_e64 v30, v30 clamp
	v_exp_f32_e64 v31, v31 clamp
	v_exp_f32_e32 v36, v44
	v_exp_f32_e32 v37, v45
	v_exp_f32_e32 v28, v28
	v_exp_f32_e32 v29, v29
	v_exp_f32_e64 v32, v32 clamp
	v_exp_f32_e64 v33, v33 clamp
	v_exp_f32_e32 v44, v46
	v_exp_f32_e32 v45, v47
	v_pk_fma_f32 v[58:59], v[80:81], s[2:3], 1.0 op_sel_hi:[1,0,0]
	v_pk_fma_f32 v[60:61], v[82:83], s[2:3], 1.0 op_sel_hi:[1,0,0]
	v_pk_fma_f32 v[52:53], v[52:53], s[2:3], 1.0 op_sel_hi:[1,0,0]
	v_pk_fma_f32 v[22:23], v[22:23], s[2:3], 1.0 op_sel_hi:[1,0,0]
	v_pk_fma_f32 v[54:55], v[54:55], s[2:3], 1.0 op_sel_hi:[1,0,0]
	v_pk_fma_f32 v[56:57], v[56:57], s[2:3], 1.0 op_sel_hi:[1,0,0]
	v_pk_fma_f32 v[30:31], v[30:31], s[2:3], 1.0 op_sel_hi:[1,0,0]
	v_pk_fma_f32 v[32:33], v[32:33], s[2:3], 1.0 op_sel_hi:[1,0,0]
	v_pk_fma_f32 v[46:47], v[78:79], v[58:59], v[58:59]
	v_pk_fma_f32 v[48:49], v[48:49], v[60:61], v[60:61]
	v_pk_fma_f32 v[50:51], v[50:51], v[52:53], v[52:53]
	v_pk_fma_f32 v[20:21], v[20:21], v[22:23], v[22:23]
	v_pk_fma_f32 v[24:25], v[24:25], v[54:55], v[54:55]
	v_pk_fma_f32 v[34:35], v[34:35], v[56:57], v[56:57]
	v_pk_fma_f32 v[26:27], v[26:27], v[30:31], v[30:31]
	v_pk_fma_f32 v[28:29], v[28:29], v[32:33], v[32:33]
	v_pk_fma_f32 v[58:59], v[58:59], s[6:7], v[40:41] op_sel_hi:[1,0,0] neg_lo:[1,0,0] neg_hi:[1,0,0]
	v_pk_fma_f32 v[60:61], v[60:61], s[6:7], v[40:41] op_sel_hi:[1,0,0] neg_lo:[1,0,0] neg_hi:[1,0,0]
	v_pk_fma_f32 v[52:53], v[52:53], s[6:7], v[40:41] op_sel_hi:[1,0,0] neg_lo:[1,0,0] neg_hi:[1,0,0]
	v_pk_fma_f32 v[22:23], v[22:23], s[6:7], v[40:41] op_sel_hi:[1,0,0] neg_lo:[1,0,0] neg_hi:[1,0,0]
	v_pk_fma_f32 v[54:55], v[54:55], s[6:7], v[40:41] op_sel_hi:[1,0,0] neg_lo:[1,0,0] neg_hi:[1,0,0]
	v_pk_fma_f32 v[56:57], v[56:57], s[6:7], v[40:41] op_sel_hi:[1,0,0] neg_lo:[1,0,0] neg_hi:[1,0,0]
	v_pk_fma_f32 v[30:31], v[30:31], s[6:7], v[40:41] op_sel_hi:[1,0,0] neg_lo:[1,0,0] neg_hi:[1,0,0]
	v_pk_fma_f32 v[32:33], v[32:33], s[6:7], v[40:41] op_sel_hi:[1,0,0] neg_lo:[1,0,0] neg_hi:[1,0,0]
	v_pk_fma_f32 v[46:47], v[4:5], v[46:47], v[46:47]
	v_pk_fma_f32 v[48:49], v[6:7], v[48:49], v[48:49]
	v_pk_fma_f32 v[50:51], v[8:9], v[50:51], v[50:51]
	v_pk_fma_f32 v[20:21], v[10:11], v[20:21], v[20:21]
	v_pk_fma_f32 v[24:25], v[12:13], v[24:25], v[24:25]
	v_pk_fma_f32 v[34:35], v[18:19], v[34:35], v[34:35]
	v_pk_fma_f32 v[26:27], v[36:37], v[26:27], v[26:27]
	v_pk_fma_f32 v[28:29], v[44:45], v[28:29], v[28:29]
	v_rcp_f32_e64 v46, v46 clamp
	v_rcp_f32_e64 v47, v47 clamp
	v_rcp_f32_e64 v48, v48 clamp
	v_rcp_f32_e64 v49, v49 clamp
	v_rcp_f32_e64 v50, v50 clamp
	v_rcp_f32_e64 v51, v51 clamp
	v_rcp_f32_e64 v20, v20 clamp
	v_rcp_f32_e64 v21, v21 clamp
	v_rcp_f32_e64 v24, v24 clamp
	v_rcp_f32_e64 v25, v25 clamp
	v_rcp_f32_e64 v34, v34 clamp
	v_rcp_f32_e64 v35, v35 clamp
	v_rcp_f32_e64 v26, v26 clamp
	v_rcp_f32_e64 v27, v27 clamp
	v_rcp_f32_e64 v28, v28 clamp
	v_rcp_f32_e64 v29, v29 clamp
	v_pk_mul_f32 v[46:47], v[58:59], v[46:47]
	v_pk_mul_f32 v[48:49], v[60:61], v[48:49]
	v_pk_mul_f32 v[50:51], v[52:53], v[50:51]
	v_pk_mul_f32 v[20:21], v[22:23], v[20:21]
	v_pk_mul_f32 v[22:23], v[54:55], v[24:25]
	v_pk_mul_f32 v[24:25], v[56:57], v[34:35]
	v_pk_mul_f32 v[26:27], v[30:31], v[26:27]
	v_pk_mul_f32 v[28:29], v[32:33], v[28:29]
	v_pk_fma_f32 v[4:5], v[4:5], v[46:47], v[46:47]
	v_pk_fma_f32 v[6:7], v[6:7], v[48:49], v[48:49]
	v_pk_fma_f32 v[8:9], v[8:9], v[50:51], v[50:51]
	v_pk_fma_f32 v[10:11], v[10:11], v[20:21], v[20:21]
	v_pk_fma_f32 v[12:13], v[12:13], v[22:23], v[22:23]
	v_pk_fma_f32 v[18:19], v[18:19], v[24:25], v[24:25]
	v_pk_fma_f32 v[30:31], v[36:37], v[26:27], v[26:27]
	v_pk_fma_f32 v[32:33], v[44:45], v[28:29], v[28:29]
	s_nop 0
	v_pk_fma_f32 v[4:5], v[4:5], v[4:5], s[4:5] neg_lo:[1,0,0] neg_hi:[1,0,0] clamp
	v_pk_fma_f32 v[6:7], v[6:7], v[6:7], s[4:5] neg_lo:[1,0,0] neg_hi:[1,0,0] clamp
	v_pk_fma_f32 v[8:9], v[8:9], v[8:9], s[4:5] neg_lo:[1,0,0] neg_hi:[1,0,0] clamp
	v_pk_fma_f32 v[10:11], v[10:11], v[10:11], s[4:5] neg_lo:[1,0,0] neg_hi:[1,0,0] clamp
	v_pk_fma_f32 v[12:13], v[12:13], v[12:13], s[4:5] neg_lo:[1,0,0] neg_hi:[1,0,0] clamp
	v_pk_fma_f32 v[18:19], v[18:19], v[18:19], s[4:5] neg_lo:[1,0,0] neg_hi:[1,0,0] clamp
	v_pk_fma_f32 v[30:31], v[30:31], v[30:31], s[4:5] neg_lo:[1,0,0] neg_hi:[1,0,0] clamp
	s_nop 0
	v_pk_fma_f32 v[32:33], v[32:33], v[32:33], s[4:5] neg_lo:[1,0,0] neg_hi:[1,0,0] clamp
	s_nop 0
	v_pk_fma_f32 v[8:9], v[8:9], v[8:9], s[8:9] op_sel_hi:[1,1,0]
	v_pk_fma_f32 v[10:11], v[10:11], v[10:11], s[8:9] op_sel_hi:[1,1,0]
	v_pk_fma_f32 v[12:13], v[12:13], v[12:13], s[8:9] op_sel_hi:[1,1,0]
	v_pk_fma_f32 v[18:19], v[18:19], v[18:19], s[8:9] op_sel_hi:[1,1,0]
	v_pk_fma_f32 v[32:33], v[32:33], v[32:33], s[8:9] op_sel_hi:[1,1,0]
	v_pk_fma_f32 v[4:5], v[4:5], v[4:5], s[8:9] op_sel_hi:[1,1,0]
	v_pk_fma_f32 v[6:7], v[6:7], v[6:7], s[8:9] op_sel_hi:[1,1,0]
	v_pk_fma_f32 v[30:31], v[30:31], v[30:31], s[8:9] op_sel_hi:[1,1,0]
	v_pk_mul_f32 v[8:9], v[50:51], v[8:9]
	v_pk_mul_f32 v[84:85], v[20:21], v[10:11]
	v_pk_mul_f32 v[86:87], v[22:23], v[12:13]
	v_pk_mul_f32 v[10:11], v[24:25], v[18:19]
	v_pk_mul_f32 v[12:13], v[28:29], v[32:33]
	v_pk_mul_f32 v[64:65], v[46:47], v[4:5]
	v_pk_mul_f32 v[82:83], v[48:49], v[6:7]
	v_pk_mul_f32 v[20:21], v[30:31], v[26:27]
	ds_read_b128 v[4:7], v72 offset:6144
	ds_read_b128 v[22:25], v71 offset:42368
	ds_read_b128 v[26:29], v72 offset:7168
	ds_read_b128 v[30:33], v71 offset:42432
	v_cvt_pk_f16_f32 v19, v84, v85
	v_cvt_pk_f16_f32 v18, v8, v9
	v_cvt_pk_f16_f32 v20, v20, v21
	v_cvt_pk_f16_f32 v21, v12, v13
	s_waitcnt lgkmcnt(2)
	v_mfma_f32_16x16x32_f16 v[34:37], v[4:7], v[14:17], v[22:25]
	v_mfma_f32_16x16x32_f16 v[44:47], v[4:7], v[0:3], v[22:25]
	ds_read_b128 v[4:7], v72 offset:8192
	ds_read_b128 v[48:51], v71 offset:42496
	s_waitcnt lgkmcnt(2)
	v_mfma_f32_16x16x32_f16 v[52:55], v[26:29], v[14:17], v[30:33]
	v_cvt_pk_f16_f32 v22, v64, v65
	v_cvt_pk_f16_f32 v23, v82, v83
	v_cvt_pk_f16_f32 v24, v86, v87
	v_mfma_f32_16x16x32_f16 v[26:29], v[26:29], v[0:3], v[30:33]
	ds_read_b128 v[56:59], v71 offset:42560
	v_exp_f32_e32 v86, v34
	v_exp_f32_e32 v87, v35
	ds_read_b128 v[30:33], v72 offset:9216
	s_waitcnt lgkmcnt(2)
	v_mfma_f32_16x16x32_f16 v[60:63], v[4:7], v[14:17], v[48:51]
	v_exp_f32_e64 v88, v52 clamp
	v_exp_f32_e64 v89, v53 clamp
	v_exp_f32_e64 v90, v54 clamp
	v_mfma_f32_16x16x32_f16 v[48:51], v[4:7], v[0:3], v[48:51]
	ds_read_b128 v[64:67], v72 offset:10240
	ds_read_b128 v[74:77], v71 offset:42624
	s_nop 1
	v_exp_f32_e32 v4, v60
	s_waitcnt lgkmcnt(2)
	v_mfma_f32_16x16x32_f16 v[78:81], v[30:33], v[14:17], v[56:59]
	v_exp_f32_e32 v5, v61
	v_exp_f32_e32 v60, v36
	v_exp_f32_e32 v61, v37
	v_mfma_f32_16x16x32_f16 v[30:33], v[30:33], v[0:3], v[56:59]
	ds_read_b128 v[82:85], v71 offset:42688
	v_exp_f32_e64 v91, v55 clamp
	v_exp_f32_e32 v6, v62
	ds_read_b128 v[56:59], v72 offset:11264
	s_waitcnt lgkmcnt(2)
	v_mfma_f32_16x16x32_f16 v[34:37], v[64:67], v[14:17], v[74:77]
	v_exp_f32_e32 v7, v63
	v_exp_f32_e32 v8, v48
	v_exp_f32_e32 v9, v49
	v_mfma_f32_16x16x32_f16 v[52:55], v[64:67], v[0:3], v[74:77]
	v_exp_f32_e32 v44, v44
	v_exp_f32_e32 v45, v45
	v_exp_f32_e64 v26, v26 clamp
	s_waitcnt lgkmcnt(0)
	v_mfma_f32_16x16x32_f16 v[14:17], v[56:59], v[14:17], v[82:85]
	v_exp_f32_e64 v27, v27 clamp
	v_exp_f32_e32 v46, v46
	v_exp_f32_e32 v47, v47
	v_mfma_f32_16x16x32_f16 v[56:59], v[56:59], v[0:3], v[82:85]
	v_exp_f32_e64 v28, v28 clamp
	s_nop 2
	v_exp_f32_e32 v2, v14
	v_exp_f32_e32 v3, v15
	v_exp_f32_e32 v14, v16
	v_exp_f32_e32 v15, v17
	v_exp_f32_e32 v16, v30
	v_exp_f32_e32 v17, v31
	v_exp_f32_e64 v29, v29 clamp
	v_exp_f32_e32 v0, v50
	v_exp_f32_e32 v1, v51
	v_exp_f32_e32 v48, v78
	v_exp_f32_e32 v49, v79
	v_exp_f32_e64 v34, v34 clamp
	v_exp_f32_e64 v35, v35 clamp
	v_exp_f32_e32 v50, v80
	v_exp_f32_e32 v51, v81
	v_exp_f32_e64 v36, v36 clamp
	v_exp_f32_e64 v37, v37 clamp
	v_exp_f32_e64 v30, v52 clamp
	v_exp_f32_e64 v31, v53 clamp
	v_exp_f32_e32 v52, v56
	v_exp_f32_e32 v53, v57
	v_exp_f32_e32 v32, v32
	v_exp_f32_e32 v33, v33
	v_exp_f32_e64 v54, v54 clamp
	v_exp_f32_e64 v55, v55 clamp
	v_exp_f32_e32 v56, v58
	v_cvt_pk_f16_f32 v25, v10, v11
	v_exp_f32_e32 v57, v59
	v_pk_fma_f32 v[30:31], v[30:31], s[2:3], 1.0 op_sel_hi:[1,0,0]
	v_pk_fma_f32 v[10:11], v[88:89], s[2:3], 1.0 op_sel_hi:[1,0,0]
	v_pk_fma_f32 v[12:13], v[90:91], s[2:3], 1.0 op_sel_hi:[1,0,0]
	v_pk_fma_f32 v[26:27], v[26:27], s[2:3], 1.0 op_sel_hi:[1,0,0]
	v_pk_fma_f32 v[28:29], v[28:29], s[2:3], 1.0 op_sel_hi:[1,0,0]
	v_pk_fma_f32 v[34:35], v[34:35], s[2:3], 1.0 op_sel_hi:[1,0,0]
	v_pk_fma_f32 v[36:37], v[36:37], s[2:3], 1.0 op_sel_hi:[1,0,0]
	v_pk_fma_f32 v[54:55], v[54:55], s[2:3], 1.0 op_sel_hi:[1,0,0]
	v_pk_fma_f32 v[16:17], v[16:17], v[30:31], v[30:31]
	v_pk_fma_f32 v[58:59], v[86:87], v[10:11], v[10:11]
	v_pk_fma_f32 v[10:11], v[10:11], s[6:7], v[40:41] op_sel_hi:[1,0,0] neg_lo:[1,0,0] neg_hi:[1,0,0]
	v_pk_fma_f32 v[60:61], v[60:61], v[12:13], v[12:13]
	v_pk_fma_f32 v[12:13], v[12:13], s[6:7], v[40:41] op_sel_hi:[1,0,0] neg_lo:[1,0,0] neg_hi:[1,0,0]
	v_pk_fma_f32 v[44:45], v[44:45], v[26:27], v[26:27]
	v_pk_fma_f32 v[46:47], v[46:47], v[28:29], v[28:29]
	v_pk_fma_f32 v[48:49], v[48:49], v[34:35], v[34:35]
	v_pk_fma_f32 v[50:51], v[50:51], v[36:37], v[36:37]
	v_pk_fma_f32 v[32:33], v[32:33], v[54:55], v[54:55]
	v_pk_fma_f32 v[16:17], v[52:53], v[16:17], v[16:17]
	v_pk_fma_f32 v[26:27], v[26:27], s[6:7], v[40:41] op_sel_hi:[1,0,0] neg_lo:[1,0,0] neg_hi:[1,0,0]
	v_pk_fma_f32 v[28:29], v[28:29], s[6:7], v[40:41] op_sel_hi:[1,0,0] neg_lo:[1,0,0] neg_hi:[1,0,0]
	v_pk_fma_f32 v[34:35], v[34:35], s[6:7], v[40:41] op_sel_hi:[1,0,0] neg_lo:[1,0,0] neg_hi:[1,0,0]
	v_pk_fma_f32 v[36:37], v[36:37], s[6:7], v[40:41] op_sel_hi:[1,0,0] neg_lo:[1,0,0] neg_hi:[1,0,0]
	v_pk_fma_f32 v[30:31], v[30:31], s[6:7], v[40:41] op_sel_hi:[1,0,0] neg_lo:[1,0,0] neg_hi:[1,0,0]
	v_pk_fma_f32 v[54:55], v[54:55], s[6:7], v[40:41] op_sel_hi:[1,0,0] neg_lo:[1,0,0] neg_hi:[1,0,0]
	v_pk_fma_f32 v[58:59], v[4:5], v[58:59], v[58:59]
	v_pk_fma_f32 v[60:61], v[6:7], v[60:61], v[60:61]
	v_pk_fma_f32 v[44:45], v[8:9], v[44:45], v[44:45]
	v_pk_fma_f32 v[46:47], v[0:1], v[46:47], v[46:47]
	v_pk_fma_f32 v[48:49], v[2:3], v[48:49], v[48:49]
	v_pk_fma_f32 v[50:51], v[14:15], v[50:51], v[50:51]
	v_pk_fma_f32 v[32:33], v[56:57], v[32:33], v[32:33]
	v_rcp_f32_e64 v16, v16 clamp
	v_rcp_f32_e64 v17, v17 clamp
	v_rcp_f32_e64 v58, v58 clamp
	v_rcp_f32_e64 v59, v59 clamp
	v_rcp_f32_e64 v60, v60 clamp
	v_rcp_f32_e64 v61, v61 clamp
	v_rcp_f32_e64 v44, v44 clamp
	v_rcp_f32_e64 v45, v45 clamp
	v_rcp_f32_e64 v46, v46 clamp
	v_rcp_f32_e64 v47, v47 clamp
	v_rcp_f32_e64 v48, v48 clamp
	v_rcp_f32_e64 v49, v49 clamp
	v_rcp_f32_e64 v50, v50 clamp
	v_rcp_f32_e64 v51, v51 clamp
	v_rcp_f32_e64 v32, v32 clamp
	v_rcp_f32_e64 v33, v33 clamp
	v_pk_mul_f32 v[10:11], v[10:11], v[58:59]
	v_pk_mul_f32 v[12:13], v[12:13], v[60:61]
	v_pk_mul_f32 v[26:27], v[26:27], v[44:45]
	v_pk_mul_f32 v[34:35], v[34:35], v[48:49]
	v_pk_mul_f32 v[36:37], v[36:37], v[50:51]
	v_pk_mul_f32 v[28:29], v[28:29], v[46:47]
	v_pk_mul_f32 v[16:17], v[30:31], v[16:17]
	v_pk_mul_f32 v[30:31], v[54:55], v[32:33]
	v_pk_fma_f32 v[4:5], v[4:5], v[10:11], v[10:11]
	v_pk_fma_f32 v[6:7], v[6:7], v[12:13], v[12:13]
	v_pk_fma_f32 v[8:9], v[8:9], v[26:27], v[26:27]
	v_pk_fma_f32 v[2:3], v[2:3], v[34:35], v[34:35]
	v_pk_fma_f32 v[14:15], v[14:15], v[36:37], v[36:37]
	v_pk_fma_f32 v[0:1], v[0:1], v[28:29], v[28:29]
	v_pk_fma_f32 v[32:33], v[52:53], v[16:17], v[16:17]
	v_pk_fma_f32 v[44:45], v[56:57], v[30:31], v[30:31]
	s_nop 0
	v_pk_fma_f32 v[4:5], v[4:5], v[4:5], s[4:5] neg_lo:[1,0,0] neg_hi:[1,0,0] clamp
	v_pk_fma_f32 v[6:7], v[6:7], v[6:7], s[4:5] neg_lo:[1,0,0] neg_hi:[1,0,0] clamp
	v_pk_fma_f32 v[8:9], v[8:9], v[8:9], s[4:5] neg_lo:[1,0,0] neg_hi:[1,0,0] clamp
	v_pk_fma_f32 v[0:1], v[0:1], v[0:1], s[4:5] neg_lo:[1,0,0] neg_hi:[1,0,0] clamp
	v_pk_fma_f32 v[2:3], v[2:3], v[2:3], s[4:5] neg_lo:[1,0,0] neg_hi:[1,0,0] clamp
	v_pk_fma_f32 v[14:15], v[14:15], v[14:15], s[4:5] neg_lo:[1,0,0] neg_hi:[1,0,0] clamp
	v_pk_fma_f32 v[32:33], v[32:33], v[32:33], s[4:5] neg_lo:[1,0,0] neg_hi:[1,0,0] clamp
	s_nop 0
	v_pk_fma_f32 v[44:45], v[44:45], v[44:45], s[4:5] neg_lo:[1,0,0] neg_hi:[1,0,0] clamp
	s_nop 0
	v_pk_fma_f32 v[32:33], v[32:33], v[32:33], s[8:9] op_sel_hi:[1,1,0]
	v_pk_fma_f32 v[4:5], v[4:5], v[4:5], s[8:9] op_sel_hi:[1,1,0]
	v_pk_fma_f32 v[6:7], v[6:7], v[6:7], s[8:9] op_sel_hi:[1,1,0]
	v_pk_fma_f32 v[8:9], v[8:9], v[8:9], s[8:9] op_sel_hi:[1,1,0]
	v_pk_fma_f32 v[0:1], v[0:1], v[0:1], s[8:9] op_sel_hi:[1,1,0]
	v_pk_fma_f32 v[2:3], v[2:3], v[2:3], s[8:9] op_sel_hi:[1,1,0]
	v_pk_fma_f32 v[14:15], v[14:15], v[14:15], s[8:9] op_sel_hi:[1,1,0]
	v_pk_fma_f32 v[44:45], v[44:45], v[44:45], s[8:9] op_sel_hi:[1,1,0]
	v_pk_mul_f32 v[16:17], v[32:33], v[16:17]
	v_pk_mul_f32 v[52:53], v[10:11], v[4:5]
	v_pk_mul_f32 v[54:55], v[12:13], v[6:7]
	v_pk_mul_f32 v[26:27], v[26:27], v[8:9]
	v_pk_mul_f32 v[28:29], v[28:29], v[0:1]
	v_pk_mul_f32 v[56:57], v[34:35], v[2:3]
	v_pk_mul_f32 v[58:59], v[36:37], v[14:15]
	v_pk_mul_f32 v[60:61], v[30:31], v[44:45]
	s_cmp_lt_u32 s33, 8
	s_cbranch_scc1 .Lprio_half
	s_setprio 0
